# adaLN inner loop rewritten with double-buffered global loads (32 in flight per lane), same fma order; on top of deferred weight conversion
# baseline (speedup 1.0000x reference)
.LBB0_20:
	v_readfirstlane_b32 s2, v54
	v_readfirstlane_b32 s3, v55
	v_subrev_u32_e32 v0, s2, v54
	s_mov_b32 vcc_lo, 0
	s_nop 4
	global_load_dword v104, v0, s[2:3]
	s_add_u32 s2, s2, 0x6000
	s_addc_u32 s3, s3, 0
	global_load_dword v105, v0, s[2:3]
	s_add_u32 s2, s2, 0x6000
	s_addc_u32 s3, s3, 0
	global_load_dword v106, v0, s[2:3]
	s_add_u32 s2, s2, 0x6000
	s_addc_u32 s3, s3, 0
	global_load_dword v107, v0, s[2:3]
	s_add_u32 s2, s2, 0x6000
	s_addc_u32 s3, s3, 0
	global_load_dword v108, v0, s[2:3]
	s_add_u32 s2, s2, 0x6000
	s_addc_u32 s3, s3, 0
	global_load_dword v109, v0, s[2:3]
	s_add_u32 s2, s2, 0x6000
	s_addc_u32 s3, s3, 0
	global_load_dword v110, v0, s[2:3]
	s_add_u32 s2, s2, 0x6000
	s_addc_u32 s3, s3, 0
	global_load_dword v111, v0, s[2:3]
	s_add_u32 s2, s2, 0x6000
	s_addc_u32 s3, s3, 0
	global_load_dword v112, v0, s[2:3]
	s_add_u32 s2, s2, 0x6000
	s_addc_u32 s3, s3, 0
	global_load_dword v113, v0, s[2:3]
	s_add_u32 s2, s2, 0x6000
	s_addc_u32 s3, s3, 0
	global_load_dword v114, v0, s[2:3]
	s_add_u32 s2, s2, 0x6000
	s_addc_u32 s3, s3, 0
	global_load_dword v115, v0, s[2:3]
	s_add_u32 s2, s2, 0x6000
	s_addc_u32 s3, s3, 0
	global_load_dword v116, v0, s[2:3]
	s_add_u32 s2, s2, 0x6000
	s_addc_u32 s3, s3, 0
	global_load_dword v117, v0, s[2:3]
	s_add_u32 s2, s2, 0x6000
	s_addc_u32 s3, s3, 0
	global_load_dword v118, v0, s[2:3]
	s_add_u32 s2, s2, 0x6000
	s_addc_u32 s3, s3, 0
	global_load_dword v119, v0, s[2:3]
	s_add_u32 s2, s2, 0x6000
	s_addc_u32 s3, s3, 0
.Ladaln_loop:
	global_load_dword v120, v0, s[2:3]
	s_add_u32 s2, s2, 0x6000
	s_addc_u32 s3, s3, 0
	global_load_dword v121, v0, s[2:3]
	s_add_u32 s2, s2, 0x6000
	s_addc_u32 s3, s3, 0
	global_load_dword v122, v0, s[2:3]
	s_add_u32 s2, s2, 0x6000
	s_addc_u32 s3, s3, 0
	global_load_dword v123, v0, s[2:3]
	s_add_u32 s2, s2, 0x6000
	s_addc_u32 s3, s3, 0
	global_load_dword v124, v0, s[2:3]
	s_add_u32 s2, s2, 0x6000
	s_addc_u32 s3, s3, 0
	global_load_dword v125, v0, s[2:3]
	s_add_u32 s2, s2, 0x6000
	s_addc_u32 s3, s3, 0
	global_load_dword v126, v0, s[2:3]
	s_add_u32 s2, s2, 0x6000
	s_addc_u32 s3, s3, 0
	global_load_dword v127, v0, s[2:3]
	s_add_u32 s2, s2, 0x6000
	s_addc_u32 s3, s3, 0
	global_load_dword v128, v0, s[2:3]
	s_add_u32 s2, s2, 0x6000
	s_addc_u32 s3, s3, 0
	global_load_dword v129, v0, s[2:3]
	s_add_u32 s2, s2, 0x6000
	s_addc_u32 s3, s3, 0
	global_load_dword v130, v0, s[2:3]
	s_add_u32 s2, s2, 0x6000
	s_addc_u32 s3, s3, 0
	global_load_dword v131, v0, s[2:3]
	s_add_u32 s2, s2, 0x6000
	s_addc_u32 s3, s3, 0
	global_load_dword v132, v0, s[2:3]
	s_add_u32 s2, s2, 0x6000
	s_addc_u32 s3, s3, 0
	global_load_dword v133, v0, s[2:3]
	s_add_u32 s2, s2, 0x6000
	s_addc_u32 s3, s3, 0
	global_load_dword v60, v0, s[2:3]
	s_add_u32 s2, s2, 0x6000
	s_addc_u32 s3, s3, 0
	global_load_dword v61, v0, s[2:3]
	s_add_u32 s2, s2, 0x6000
	s_addc_u32 s3, s3, 0
	ds_read_b128 v[2:5], v67
	ds_read_b128 v[6:9], v67 offset:16
	ds_read_b128 v[10:13], v67 offset:32
	ds_read_b128 v[14:17], v67 offset:48
	ds_read_b128 v[18:21], v67 offset:4096
	ds_read_b128 v[22:25], v67 offset:4112
	ds_read_b128 v[26:29], v67 offset:4128
	ds_read_b128 v[30:33], v67 offset:4144
	ds_read_b128 v[34:37], v67 offset:8192
	ds_read_b128 v[38:41], v67 offset:8208
	ds_read_b128 v[42:45], v67 offset:8224
	ds_read_b128 v[68:71], v67 offset:8240
	ds_read_b128 v[72:75], v67 offset:12288
	ds_read_b128 v[76:79], v67 offset:12304
	ds_read_b128 v[80:83], v67 offset:12320
	ds_read_b128 v[84:87], v67 offset:12336
	ds_read_b128 v[88:91], v67 offset:16384
	ds_read_b128 v[92:95], v67 offset:16400
	ds_read_b128 v[96:99], v67 offset:16416
	ds_read_b128 v[100:103], v67 offset:16432
	v_add_u32_e32 v67, 64, v67
	s_waitcnt lgkmcnt(0)
	s_waitcnt vmcnt(31)
	v_fmac_f32_e32 v56, v104, v2
	v_fmac_f32_e32 v57, v104, v18
	v_fmac_f32_e32 v58, v104, v34
	v_fmac_f32_e32 v59, v104, v72
	v_fmac_f32_e32 v66, v104, v88
	s_waitcnt vmcnt(30)
	v_fmac_f32_e32 v56, v105, v3
	v_fmac_f32_e32 v57, v105, v19
	v_fmac_f32_e32 v58, v105, v35
	v_fmac_f32_e32 v59, v105, v73
	v_fmac_f32_e32 v66, v105, v89
	s_waitcnt vmcnt(29)
	v_fmac_f32_e32 v56, v106, v4
	v_fmac_f32_e32 v57, v106, v20
	v_fmac_f32_e32 v58, v106, v36
	v_fmac_f32_e32 v59, v106, v74
	v_fmac_f32_e32 v66, v106, v90
	s_waitcnt vmcnt(28)
	v_fmac_f32_e32 v56, v107, v5
	v_fmac_f32_e32 v57, v107, v21
	v_fmac_f32_e32 v58, v107, v37
	v_fmac_f32_e32 v59, v107, v75
	v_fmac_f32_e32 v66, v107, v91
	s_waitcnt vmcnt(27)
	v_fmac_f32_e32 v56, v108, v6
	v_fmac_f32_e32 v57, v108, v22
	v_fmac_f32_e32 v58, v108, v38
	v_fmac_f32_e32 v59, v108, v76
	v_fmac_f32_e32 v66, v108, v92
	s_waitcnt vmcnt(26)
	v_fmac_f32_e32 v56, v109, v7
	v_fmac_f32_e32 v57, v109, v23
	v_fmac_f32_e32 v58, v109, v39
	v_fmac_f32_e32 v59, v109, v77
	v_fmac_f32_e32 v66, v109, v93
	s_waitcnt vmcnt(25)
	v_fmac_f32_e32 v56, v110, v8
	v_fmac_f32_e32 v57, v110, v24
	v_fmac_f32_e32 v58, v110, v40
	v_fmac_f32_e32 v59, v110, v78
	v_fmac_f32_e32 v66, v110, v94
	s_waitcnt vmcnt(24)
	v_fmac_f32_e32 v56, v111, v9
	v_fmac_f32_e32 v57, v111, v25
	v_fmac_f32_e32 v58, v111, v41
	v_fmac_f32_e32 v59, v111, v79
	v_fmac_f32_e32 v66, v111, v95
	s_waitcnt vmcnt(23)
	v_fmac_f32_e32 v56, v112, v10
	v_fmac_f32_e32 v57, v112, v26
	v_fmac_f32_e32 v58, v112, v42
	v_fmac_f32_e32 v59, v112, v80
	v_fmac_f32_e32 v66, v112, v96
	s_waitcnt vmcnt(22)
	v_fmac_f32_e32 v56, v113, v11
	v_fmac_f32_e32 v57, v113, v27
	v_fmac_f32_e32 v58, v113, v43
	v_fmac_f32_e32 v59, v113, v81
	v_fmac_f32_e32 v66, v113, v97
	s_waitcnt vmcnt(21)
	v_fmac_f32_e32 v56, v114, v12
	v_fmac_f32_e32 v57, v114, v28
	v_fmac_f32_e32 v58, v114, v44
	v_fmac_f32_e32 v59, v114, v82
	v_fmac_f32_e32 v66, v114, v98
	s_waitcnt vmcnt(20)
	v_fmac_f32_e32 v56, v115, v13
	v_fmac_f32_e32 v57, v115, v29
	v_fmac_f32_e32 v58, v115, v45
	v_fmac_f32_e32 v59, v115, v83
	v_fmac_f32_e32 v66, v115, v99
	s_waitcnt vmcnt(19)
	v_fmac_f32_e32 v56, v116, v14
	v_fmac_f32_e32 v57, v116, v30
	v_fmac_f32_e32 v58, v116, v68
	v_fmac_f32_e32 v59, v116, v84
	v_fmac_f32_e32 v66, v116, v100
	s_waitcnt vmcnt(18)
	v_fmac_f32_e32 v56, v117, v15
	v_fmac_f32_e32 v57, v117, v31
	v_fmac_f32_e32 v58, v117, v69
	v_fmac_f32_e32 v59, v117, v85
	v_fmac_f32_e32 v66, v117, v101
	s_waitcnt vmcnt(17)
	v_fmac_f32_e32 v56, v118, v16
	v_fmac_f32_e32 v57, v118, v32
	v_fmac_f32_e32 v58, v118, v70
	v_fmac_f32_e32 v59, v118, v86
	v_fmac_f32_e32 v66, v118, v102
	s_waitcnt vmcnt(16)
	v_fmac_f32_e32 v56, v119, v17
	v_fmac_f32_e32 v57, v119, v33
	v_fmac_f32_e32 v58, v119, v71
	v_fmac_f32_e32 v59, v119, v87
	v_fmac_f32_e32 v66, v119, v103
	global_load_dword v104, v0, s[2:3]
	s_add_u32 s2, s2, 0x6000
	s_addc_u32 s3, s3, 0
	global_load_dword v105, v0, s[2:3]
	s_add_u32 s2, s2, 0x6000
	s_addc_u32 s3, s3, 0
	global_load_dword v106, v0, s[2:3]
	s_add_u32 s2, s2, 0x6000
	s_addc_u32 s3, s3, 0
	global_load_dword v107, v0, s[2:3]
	s_add_u32 s2, s2, 0x6000
	s_addc_u32 s3, s3, 0
	global_load_dword v108, v0, s[2:3]
	s_add_u32 s2, s2, 0x6000
	s_addc_u32 s3, s3, 0
	global_load_dword v109, v0, s[2:3]
	s_add_u32 s2, s2, 0x6000
	s_addc_u32 s3, s3, 0
	global_load_dword v110, v0, s[2:3]
	s_add_u32 s2, s2, 0x6000
	s_addc_u32 s3, s3, 0
	global_load_dword v111, v0, s[2:3]
	s_add_u32 s2, s2, 0x6000
	s_addc_u32 s3, s3, 0
	global_load_dword v112, v0, s[2:3]
	s_add_u32 s2, s2, 0x6000
	s_addc_u32 s3, s3, 0
	global_load_dword v113, v0, s[2:3]
	s_add_u32 s2, s2, 0x6000
	s_addc_u32 s3, s3, 0
	global_load_dword v114, v0, s[2:3]
	s_add_u32 s2, s2, 0x6000
	s_addc_u32 s3, s3, 0
	global_load_dword v115, v0, s[2:3]
	s_add_u32 s2, s2, 0x6000
	s_addc_u32 s3, s3, 0
	global_load_dword v116, v0, s[2:3]
	s_add_u32 s2, s2, 0x6000
	s_addc_u32 s3, s3, 0
	global_load_dword v117, v0, s[2:3]
	s_add_u32 s2, s2, 0x6000
	s_addc_u32 s3, s3, 0
	global_load_dword v118, v0, s[2:3]
	s_add_u32 s2, s2, 0x6000
	s_addc_u32 s3, s3, 0
	global_load_dword v119, v0, s[2:3]
	s_add_u32 s2, s2, 0x6000
	s_addc_u32 s3, s3, 0
	ds_read_b128 v[2:5], v67
	ds_read_b128 v[6:9], v67 offset:16
	ds_read_b128 v[10:13], v67 offset:32
	ds_read_b128 v[14:17], v67 offset:48
	ds_read_b128 v[18:21], v67 offset:4096
	ds_read_b128 v[22:25], v67 offset:4112
	ds_read_b128 v[26:29], v67 offset:4128
	ds_read_b128 v[30:33], v67 offset:4144
	ds_read_b128 v[34:37], v67 offset:8192
	ds_read_b128 v[38:41], v67 offset:8208
	ds_read_b128 v[42:45], v67 offset:8224
	ds_read_b128 v[68:71], v67 offset:8240
	ds_read_b128 v[72:75], v67 offset:12288
	ds_read_b128 v[76:79], v67 offset:12304
	ds_read_b128 v[80:83], v67 offset:12320
	ds_read_b128 v[84:87], v67 offset:12336
	ds_read_b128 v[88:91], v67 offset:16384
	ds_read_b128 v[92:95], v67 offset:16400
	ds_read_b128 v[96:99], v67 offset:16416
	ds_read_b128 v[100:103], v67 offset:16432
	v_add_u32_e32 v67, 64, v67
	s_waitcnt lgkmcnt(0)
	s_waitcnt vmcnt(31)
	v_fmac_f32_e32 v56, v120, v2
	v_fmac_f32_e32 v57, v120, v18
	v_fmac_f32_e32 v58, v120, v34
	v_fmac_f32_e32 v59, v120, v72
	v_fmac_f32_e32 v66, v120, v88
	s_waitcnt vmcnt(30)
	v_fmac_f32_e32 v56, v121, v3
	v_fmac_f32_e32 v57, v121, v19
	v_fmac_f32_e32 v58, v121, v35
	v_fmac_f32_e32 v59, v121, v73
	v_fmac_f32_e32 v66, v121, v89
	s_waitcnt vmcnt(29)
	v_fmac_f32_e32 v56, v122, v4
	v_fmac_f32_e32 v57, v122, v20
	v_fmac_f32_e32 v58, v122, v36
	v_fmac_f32_e32 v59, v122, v74
	v_fmac_f32_e32 v66, v122, v90
	s_waitcnt vmcnt(28)
	v_fmac_f32_e32 v56, v123, v5
	v_fmac_f32_e32 v57, v123, v21
	v_fmac_f32_e32 v58, v123, v37
	v_fmac_f32_e32 v59, v123, v75
	v_fmac_f32_e32 v66, v123, v91
	s_waitcnt vmcnt(27)
	v_fmac_f32_e32 v56, v124, v6
	v_fmac_f32_e32 v57, v124, v22
	v_fmac_f32_e32 v58, v124, v38
	v_fmac_f32_e32 v59, v124, v76
	v_fmac_f32_e32 v66, v124, v92
	s_waitcnt vmcnt(26)
	v_fmac_f32_e32 v56, v125, v7
	v_fmac_f32_e32 v57, v125, v23
	v_fmac_f32_e32 v58, v125, v39
	v_fmac_f32_e32 v59, v125, v77
	v_fmac_f32_e32 v66, v125, v93
	s_waitcnt vmcnt(25)
	v_fmac_f32_e32 v56, v126, v8
	v_fmac_f32_e32 v57, v126, v24
	v_fmac_f32_e32 v58, v126, v40
	v_fmac_f32_e32 v59, v126, v78
	v_fmac_f32_e32 v66, v126, v94
	s_waitcnt vmcnt(24)
	v_fmac_f32_e32 v56, v127, v9
	v_fmac_f32_e32 v57, v127, v25
	v_fmac_f32_e32 v58, v127, v41
	v_fmac_f32_e32 v59, v127, v79
	v_fmac_f32_e32 v66, v127, v95
	s_waitcnt vmcnt(23)
	v_fmac_f32_e32 v56, v128, v10
	v_fmac_f32_e32 v57, v128, v26
	v_fmac_f32_e32 v58, v128, v42
	v_fmac_f32_e32 v59, v128, v80
	v_fmac_f32_e32 v66, v128, v96
	s_waitcnt vmcnt(22)
	v_fmac_f32_e32 v56, v129, v11
	v_fmac_f32_e32 v57, v129, v27
	v_fmac_f32_e32 v58, v129, v43
	v_fmac_f32_e32 v59, v129, v81
	v_fmac_f32_e32 v66, v129, v97
	s_waitcnt vmcnt(21)
	v_fmac_f32_e32 v56, v130, v12
	v_fmac_f32_e32 v57, v130, v28
	v_fmac_f32_e32 v58, v130, v44
	v_fmac_f32_e32 v59, v130, v82
	v_fmac_f32_e32 v66, v130, v98
	s_waitcnt vmcnt(20)
	v_fmac_f32_e32 v56, v131, v13
	v_fmac_f32_e32 v57, v131, v29
	v_fmac_f32_e32 v58, v131, v45
	v_fmac_f32_e32 v59, v131, v83
	v_fmac_f32_e32 v66, v131, v99
	s_waitcnt vmcnt(19)
	v_fmac_f32_e32 v56, v132, v14
	v_fmac_f32_e32 v57, v132, v30
	v_fmac_f32_e32 v58, v132, v68
	v_fmac_f32_e32 v59, v132, v84
	v_fmac_f32_e32 v66, v132, v100
	s_waitcnt vmcnt(18)
	v_fmac_f32_e32 v56, v133, v15
	v_fmac_f32_e32 v57, v133, v31
	v_fmac_f32_e32 v58, v133, v69
	v_fmac_f32_e32 v59, v133, v85
	v_fmac_f32_e32 v66, v133, v101
	s_waitcnt vmcnt(17)
	v_fmac_f32_e32 v56, v60, v16
	v_fmac_f32_e32 v57, v60, v32
	v_fmac_f32_e32 v58, v60, v70
	v_fmac_f32_e32 v59, v60, v86
	v_fmac_f32_e32 v66, v60, v102
	s_waitcnt vmcnt(16)
	v_fmac_f32_e32 v56, v61, v17
	v_fmac_f32_e32 v57, v61, v33
	v_fmac_f32_e32 v58, v61, v71
	v_fmac_f32_e32 v59, v61, v87
	v_fmac_f32_e32 v66, v61, v103
	s_add_i32 vcc_lo, vcc_lo, 1
	s_cmp_lt_u32 vcc_lo, 7
	s_cbranch_scc1 .Ladaln_loop
	global_load_dword v120, v0, s[2:3]
	s_add_u32 s2, s2, 0x6000
	s_addc_u32 s3, s3, 0
	global_load_dword v121, v0, s[2:3]
	s_add_u32 s2, s2, 0x6000
	s_addc_u32 s3, s3, 0
	global_load_dword v122, v0, s[2:3]
	s_add_u32 s2, s2, 0x6000
	s_addc_u32 s3, s3, 0
	global_load_dword v123, v0, s[2:3]
	s_add_u32 s2, s2, 0x6000
	s_addc_u32 s3, s3, 0
	global_load_dword v124, v0, s[2:3]
	s_add_u32 s2, s2, 0x6000
	s_addc_u32 s3, s3, 0
	global_load_dword v125, v0, s[2:3]
	s_add_u32 s2, s2, 0x6000
	s_addc_u32 s3, s3, 0
	global_load_dword v126, v0, s[2:3]
	s_add_u32 s2, s2, 0x6000
	s_addc_u32 s3, s3, 0
	global_load_dword v127, v0, s[2:3]
	s_add_u32 s2, s2, 0x6000
	s_addc_u32 s3, s3, 0
	global_load_dword v128, v0, s[2:3]
	s_add_u32 s2, s2, 0x6000
	s_addc_u32 s3, s3, 0
	global_load_dword v129, v0, s[2:3]
	s_add_u32 s2, s2, 0x6000
	s_addc_u32 s3, s3, 0
	global_load_dword v130, v0, s[2:3]
	s_add_u32 s2, s2, 0x6000
	s_addc_u32 s3, s3, 0
	global_load_dword v131, v0, s[2:3]
	s_add_u32 s2, s2, 0x6000
	s_addc_u32 s3, s3, 0
	global_load_dword v132, v0, s[2:3]
	s_add_u32 s2, s2, 0x6000
	s_addc_u32 s3, s3, 0
	global_load_dword v133, v0, s[2:3]
	s_add_u32 s2, s2, 0x6000
	s_addc_u32 s3, s3, 0
	global_load_dword v60, v0, s[2:3]
	s_add_u32 s2, s2, 0x6000
	s_addc_u32 s3, s3, 0
	global_load_dword v61, v0, s[2:3]
	s_add_u32 s2, s2, 0x6000
	s_addc_u32 s3, s3, 0
	ds_read_b128 v[2:5], v67
	ds_read_b128 v[6:9], v67 offset:16
	ds_read_b128 v[10:13], v67 offset:32
	ds_read_b128 v[14:17], v67 offset:48
	ds_read_b128 v[18:21], v67 offset:4096
	ds_read_b128 v[22:25], v67 offset:4112
	ds_read_b128 v[26:29], v67 offset:4128
	ds_read_b128 v[30:33], v67 offset:4144
	ds_read_b128 v[34:37], v67 offset:8192
	ds_read_b128 v[38:41], v67 offset:8208
	ds_read_b128 v[42:45], v67 offset:8224
	ds_read_b128 v[68:71], v67 offset:8240
	ds_read_b128 v[72:75], v67 offset:12288
	ds_read_b128 v[76:79], v67 offset:12304
	ds_read_b128 v[80:83], v67 offset:12320
	ds_read_b128 v[84:87], v67 offset:12336
	ds_read_b128 v[88:91], v67 offset:16384
	ds_read_b128 v[92:95], v67 offset:16400
	ds_read_b128 v[96:99], v67 offset:16416
	ds_read_b128 v[100:103], v67 offset:16432
	v_add_u32_e32 v67, 64, v67
	s_waitcnt lgkmcnt(0)
	s_waitcnt vmcnt(31)
	v_fmac_f32_e32 v56, v104, v2
	v_fmac_f32_e32 v57, v104, v18
	v_fmac_f32_e32 v58, v104, v34
	v_fmac_f32_e32 v59, v104, v72
	v_fmac_f32_e32 v66, v104, v88
	s_waitcnt vmcnt(30)
	v_fmac_f32_e32 v56, v105, v3
	v_fmac_f32_e32 v57, v105, v19
	v_fmac_f32_e32 v58, v105, v35
	v_fmac_f32_e32 v59, v105, v73
	v_fmac_f32_e32 v66, v105, v89
	s_waitcnt vmcnt(29)
	v_fmac_f32_e32 v56, v106, v4
	v_fmac_f32_e32 v57, v106, v20
	v_fmac_f32_e32 v58, v106, v36
	v_fmac_f32_e32 v59, v106, v74
	v_fmac_f32_e32 v66, v106, v90
	s_waitcnt vmcnt(28)
	v_fmac_f32_e32 v56, v107, v5
	v_fmac_f32_e32 v57, v107, v21
	v_fmac_f32_e32 v58, v107, v37
	v_fmac_f32_e32 v59, v107, v75
	v_fmac_f32_e32 v66, v107, v91
	s_waitcnt vmcnt(27)
	v_fmac_f32_e32 v56, v108, v6
	v_fmac_f32_e32 v57, v108, v22
	v_fmac_f32_e32 v58, v108, v38
	v_fmac_f32_e32 v59, v108, v76
	v_fmac_f32_e32 v66, v108, v92
	s_waitcnt vmcnt(26)
	v_fmac_f32_e32 v56, v109, v7
	v_fmac_f32_e32 v57, v109, v23
	v_fmac_f32_e32 v58, v109, v39
	v_fmac_f32_e32 v59, v109, v77
	v_fmac_f32_e32 v66, v109, v93
	s_waitcnt vmcnt(25)
	v_fmac_f32_e32 v56, v110, v8
	v_fmac_f32_e32 v57, v110, v24
	v_fmac_f32_e32 v58, v110, v40
	v_fmac_f32_e32 v59, v110, v78
	v_fmac_f32_e32 v66, v110, v94
	s_waitcnt vmcnt(24)
	v_fmac_f32_e32 v56, v111, v9
	v_fmac_f32_e32 v57, v111, v25
	v_fmac_f32_e32 v58, v111, v41
	v_fmac_f32_e32 v59, v111, v79
	v_fmac_f32_e32 v66, v111, v95
	s_waitcnt vmcnt(23)
	v_fmac_f32_e32 v56, v112, v10
	v_fmac_f32_e32 v57, v112, v26
	v_fmac_f32_e32 v58, v112, v42
	v_fmac_f32_e32 v59, v112, v80
	v_fmac_f32_e32 v66, v112, v96
	s_waitcnt vmcnt(22)
	v_fmac_f32_e32 v56, v113, v11
	v_fmac_f32_e32 v57, v113, v27
	v_fmac_f32_e32 v58, v113, v43
	v_fmac_f32_e32 v59, v113, v81
	v_fmac_f32_e32 v66, v113, v97
	s_waitcnt vmcnt(21)
	v_fmac_f32_e32 v56, v114, v12
	v_fmac_f32_e32 v57, v114, v28
	v_fmac_f32_e32 v58, v114, v44
	v_fmac_f32_e32 v59, v114, v82
	v_fmac_f32_e32 v66, v114, v98
	s_waitcnt vmcnt(20)
	v_fmac_f32_e32 v56, v115, v13
	v_fmac_f32_e32 v57, v115, v29
	v_fmac_f32_e32 v58, v115, v45
	v_fmac_f32_e32 v59, v115, v83
	v_fmac_f32_e32 v66, v115, v99
	s_waitcnt vmcnt(19)
	v_fmac_f32_e32 v56, v116, v14
	v_fmac_f32_e32 v57, v116, v30
	v_fmac_f32_e32 v58, v116, v68
	v_fmac_f32_e32 v59, v116, v84
	v_fmac_f32_e32 v66, v116, v100
	s_waitcnt vmcnt(18)
	v_fmac_f32_e32 v56, v117, v15
	v_fmac_f32_e32 v57, v117, v31
	v_fmac_f32_e32 v58, v117, v69
	v_fmac_f32_e32 v59, v117, v85
	v_fmac_f32_e32 v66, v117, v101
	s_waitcnt vmcnt(17)
	v_fmac_f32_e32 v56, v118, v16
	v_fmac_f32_e32 v57, v118, v32
	v_fmac_f32_e32 v58, v118, v70
	v_fmac_f32_e32 v59, v118, v86
	v_fmac_f32_e32 v66, v118, v102
	s_waitcnt vmcnt(16)
	v_fmac_f32_e32 v56, v119, v17
	v_fmac_f32_e32 v57, v119, v33
	v_fmac_f32_e32 v58, v119, v71
	v_fmac_f32_e32 v59, v119, v87
	v_fmac_f32_e32 v66, v119, v103
	ds_read_b128 v[2:5], v67
	ds_read_b128 v[6:9], v67 offset:16
	ds_read_b128 v[10:13], v67 offset:32
	ds_read_b128 v[14:17], v67 offset:48
	ds_read_b128 v[18:21], v67 offset:4096
	ds_read_b128 v[22:25], v67 offset:4112
	ds_read_b128 v[26:29], v67 offset:4128
	ds_read_b128 v[30:33], v67 offset:4144
	ds_read_b128 v[34:37], v67 offset:8192
	ds_read_b128 v[38:41], v67 offset:8208
	ds_read_b128 v[42:45], v67 offset:8224
	ds_read_b128 v[68:71], v67 offset:8240
	ds_read_b128 v[72:75], v67 offset:12288
	ds_read_b128 v[76:79], v67 offset:12304
	ds_read_b128 v[80:83], v67 offset:12320
	ds_read_b128 v[84:87], v67 offset:12336
	ds_read_b128 v[88:91], v67 offset:16384
	ds_read_b128 v[92:95], v67 offset:16400
	ds_read_b128 v[96:99], v67 offset:16416
	ds_read_b128 v[100:103], v67 offset:16432
	v_add_u32_e32 v67, 64, v67
	s_waitcnt lgkmcnt(0)
	s_waitcnt vmcnt(15)
	v_fmac_f32_e32 v56, v120, v2
	v_fmac_f32_e32 v57, v120, v18
	v_fmac_f32_e32 v58, v120, v34
	v_fmac_f32_e32 v59, v120, v72
	v_fmac_f32_e32 v66, v120, v88
	s_waitcnt vmcnt(14)
	v_fmac_f32_e32 v56, v121, v3
	v_fmac_f32_e32 v57, v121, v19
	v_fmac_f32_e32 v58, v121, v35
	v_fmac_f32_e32 v59, v121, v73
	v_fmac_f32_e32 v66, v121, v89
	s_waitcnt vmcnt(13)
	v_fmac_f32_e32 v56, v122, v4
	v_fmac_f32_e32 v57, v122, v20
	v_fmac_f32_e32 v58, v122, v36
	v_fmac_f32_e32 v59, v122, v74
	v_fmac_f32_e32 v66, v122, v90
	s_waitcnt vmcnt(12)
	v_fmac_f32_e32 v56, v123, v5
	v_fmac_f32_e32 v57, v123, v21
	v_fmac_f32_e32 v58, v123, v37
	v_fmac_f32_e32 v59, v123, v75
	v_fmac_f32_e32 v66, v123, v91
	s_waitcnt vmcnt(11)
	v_fmac_f32_e32 v56, v124, v6
	v_fmac_f32_e32 v57, v124, v22
	v_fmac_f32_e32 v58, v124, v38
	v_fmac_f32_e32 v59, v124, v76
	v_fmac_f32_e32 v66, v124, v92
	s_waitcnt vmcnt(10)
	v_fmac_f32_e32 v56, v125, v7
	v_fmac_f32_e32 v57, v125, v23
	v_fmac_f32_e32 v58, v125, v39
	v_fmac_f32_e32 v59, v125, v77
	v_fmac_f32_e32 v66, v125, v93
	s_waitcnt vmcnt(9)
	v_fmac_f32_e32 v56, v126, v8
	v_fmac_f32_e32 v57, v126, v24
	v_fmac_f32_e32 v58, v126, v40
	v_fmac_f32_e32 v59, v126, v78
	v_fmac_f32_e32 v66, v126, v94
	s_waitcnt vmcnt(8)
	v_fmac_f32_e32 v56, v127, v9
	v_fmac_f32_e32 v57, v127, v25
	v_fmac_f32_e32 v58, v127, v41
	v_fmac_f32_e32 v59, v127, v79
	v_fmac_f32_e32 v66, v127, v95
	s_waitcnt vmcnt(7)
	v_fmac_f32_e32 v56, v128, v10
	v_fmac_f32_e32 v57, v128, v26
	v_fmac_f32_e32 v58, v128, v42
	v_fmac_f32_e32 v59, v128, v80
	v_fmac_f32_e32 v66, v128, v96
	s_waitcnt vmcnt(6)
	v_fmac_f32_e32 v56, v129, v11
	v_fmac_f32_e32 v57, v129, v27
	v_fmac_f32_e32 v58, v129, v43
	v_fmac_f32_e32 v59, v129, v81
	v_fmac_f32_e32 v66, v129, v97
	s_waitcnt vmcnt(5)
	v_fmac_f32_e32 v56, v130, v12
	v_fmac_f32_e32 v57, v130, v28
	v_fmac_f32_e32 v58, v130, v44
	v_fmac_f32_e32 v59, v130, v82
	v_fmac_f32_e32 v66, v130, v98
	s_waitcnt vmcnt(4)
	v_fmac_f32_e32 v56, v131, v13
	v_fmac_f32_e32 v57, v131, v29
	v_fmac_f32_e32 v58, v131, v45
	v_fmac_f32_e32 v59, v131, v83
	v_fmac_f32_e32 v66, v131, v99
	s_waitcnt vmcnt(3)
	v_fmac_f32_e32 v56, v132, v14
	v_fmac_f32_e32 v57, v132, v30
	v_fmac_f32_e32 v58, v132, v68
	v_fmac_f32_e32 v59, v132, v84
	v_fmac_f32_e32 v66, v132, v100
	s_waitcnt vmcnt(2)
	v_fmac_f32_e32 v56, v133, v15
	v_fmac_f32_e32 v57, v133, v31
	v_fmac_f32_e32 v58, v133, v69
	v_fmac_f32_e32 v59, v133, v85
	v_fmac_f32_e32 v66, v133, v101
	s_waitcnt vmcnt(1)
	v_fmac_f32_e32 v56, v60, v16
	v_fmac_f32_e32 v57, v60, v32
	v_fmac_f32_e32 v58, v60, v70
	v_fmac_f32_e32 v59, v60, v86
	v_fmac_f32_e32 v66, v60, v102
	s_waitcnt vmcnt(0)
	v_fmac_f32_e32 v56, v61, v17
	v_fmac_f32_e32 v57, v61, v33
	v_fmac_f32_e32 v58, v61, v71
	v_fmac_f32_e32 v59, v61, v87
	v_fmac_f32_e32 v66, v61, v103
	ds_bpermute_b32 v0, v63, v56
	ds_bpermute_b32 v3, v63, v57
	ds_bpermute_b32 v4, v63, v58
	ds_bpermute_b32 v5, v63, v59
	ds_bpermute_b32 v7, v63, v66
	s_waitcnt lgkmcnt(4)
	v_add_f32_e32 v2, v56, v0
	s_waitcnt lgkmcnt(3)
	v_add_f32_e32 v3, v57, v3
	s_waitcnt lgkmcnt(2)
	v_add_f32_e32 v4, v58, v4
	s_waitcnt lgkmcnt(1)
	v_add_f32_e32 v6, v59, v5
	s_waitcnt lgkmcnt(0)
	v_add_f32_e32 v8, v66, v7
	ds_bpermute_b32 v5, v64, v2
	ds_bpermute_b32 v7, v64, v3
	ds_bpermute_b32 v9, v64, v4
	ds_bpermute_b32 v10, v64, v6
	ds_bpermute_b32 v11, v64, v8
	s_and_saveexec_b64 s[2:3], s[0:1]
	s_cbranch_execz .LBB0_18
	s_mul_i32 s24, s23, 0x1800
	v_add_u32_e32 v12, s24, v52
	v_readlane_b32 s36, v251, 28
	v_ashrrev_i32_e32 v13, 31, v12
	v_readlane_b32 s46, v251, 38
	v_readlane_b32 s47, v251, 39
	s_mul_hi_i32 s25, s23, 0x1e000
	s_mul_i32 s23, s23, 0x1e000
	v_lshl_add_u64 v[12:13], v[12:13], 2, s[46:47]
	global_load_dword v0, v[12:13], off
	v_readlane_b32 s26, v251, 26
	v_readlane_b32 s27, v251, 27
	s_add_u32 s24, s26, s23
	s_addc_u32 s25, s27, s25
	s_waitcnt lgkmcnt(3)
	v_add_f32_e32 v15, v3, v7
	v_add_f32_e32 v16, v2, v5
	v_lshl_add_u64 v[2:3], v[52:53], 2, s[24:25]
	s_waitcnt lgkmcnt(2)
	v_add_f32_e32 v14, v4, v9
	v_add_co_u32_e32 v4, vcc, s4, v2
	s_waitcnt lgkmcnt(1)
	v_add_f32_e32 v13, v6, v10
	v_addc_co_u32_e32 v5, vcc, 0, v3, vcc
	v_add_co_u32_e32 v6, vcc, 0xc000, v2
	s_waitcnt lgkmcnt(0)
	v_add_f32_e32 v12, v8, v11
	v_addc_co_u32_e32 v7, vcc, 0, v3, vcc
	v_add_co_u32_e32 v8, vcc, 0x12000, v2
	v_readlane_b32 s37, v251, 29
	s_nop 0
	v_addc_co_u32_e32 v9, vcc, 0, v3, vcc
	v_add_co_u32_e32 v10, vcc, 0x18000, v2
	v_readlane_b32 s38, v251, 30
	v_readlane_b32 s39, v251, 31
	v_readlane_b32 s40, v251, 32
	v_readlane_b32 s41, v251, 33
	v_readlane_b32 s42, v251, 34
	v_readlane_b32 s43, v251, 35
	v_readlane_b32 s44, v251, 36
	v_readlane_b32 s45, v251, 37
	v_readlane_b32 s48, v251, 40
	v_readlane_b32 s49, v251, 41
	v_readlane_b32 s50, v251, 42
	v_readlane_b32 s51, v251, 43
	v_addc_co_u32_e32 v11, vcc, 0, v3, vcc
	s_waitcnt vmcnt(0)
	v_add_f32_e32 v16, v16, v0
	v_add_f32_e32 v15, v15, v0
	v_add_f32_e32 v14, v14, v0
	v_add_f32_e32 v13, v13, v0
	v_add_f32_e32 v0, v12, v0
	global_store_dword v[2:3], v16, off
	global_store_dword v[4:5], v15, off
	global_store_dword v[6:7], v14, off
	global_store_dword v[8:9], v13, off
	global_store_dword v[10:11], v0, off
	s_branch .LBB0_18
